# GEMM1 K-loop: loop-invariant A-fragment LDS read addresses kept in spare VGPRs; dead high-word moves dropped
# speedup vs baseline: 1.0031x; 1.0031x over previous
.LBB0_896:
	v_readlane_b32 s3, v254, 10
	s_lshl_b32 s59, s2, 6
	v_ashrrev_i32_e32 v4, 5, v2
	s_lshl_b32 s2, s2, 13
	v_lshlrev_b32_e32 v1, 1, v2
	v_lshl_add_u32 v5, v4, 10, s2
	s_lshl_b32 s2, s3, 5
	v_and_b32_e32 v3, 32, v1
	v_lshlrev_b32_e32 v2, 6, v2
	s_and_b32 s60, s2, 0x60
	v_or_b32_e32 v6, v5, v3
	v_and_b32_e32 v2, 0x3c0, v2
	v_and_b32_e32 v1, 16, v1
	s_lshr_b32 s2, s60, 3
	v_or3_b32 v6, v6, v2, v1
	v_add_lshl_u32 v4, v4, s2, 10
	v_or_b32_e32 v2, v2, v3
	v_or3_b32 v194, v2, v4, v1
	v_or_b32_e32 v2, 16, v2
	v_mov_b32_e32 v177, 0
	v_bitop3_b32 v5, v2, v5, v1 bitop3:0xde
	v_bitop3_b32 v195, v2, v4, v1 bitop3:0xde
	v_mbcnt_lo_u32_b32 v1, -1, 0
	v_mbcnt_hi_u32_b32 v1, -1, v1
	v_and_b32_e32 v4, 15, v1
	v_lshrrev_b32_e32 v1, 4, v1
	v_lshlrev_b32_e32 v1, 1, v1
	v_bfe_u32 v194, v4, 1, 3
	v_and_b32_e32 v194, 5, v194
	v_xor_b32_e32 v1, v1, v194
	v_lshlrev_b32_e32 v1, 4, v1
	v_lshl_add_u32 v1, v4, 7, v1
	v_lshl_add_u32 v6, s59, 7, v1
	v_xor_b32_e32 v5, 16, v6
	v_lshl_add_u32 v194, s60, 7, v1
	v_xor_b32_e32 v195, 16, v194
	s_waitcnt vmcnt(2)
	s_barrier
	s_mov_b64 s[14:15], 0x80
	v_lshl_add_u64 v[2:3], s[36:37], 0, v[176:177]
	s_add_i32 m0, s50, 0x18000
	v_lshl_add_u64 v[2:3], v[2:3], 0, s[14:15]
	s_add_i32 s58, s3, s49
	global_load_lds_dwordx4 v[2:3], off
	v_mov_b32_e32 v179, v177
	s_add_i32 m0, s50, 0x1a000
	s_add_u32 s2, s10, 0x36000080
	v_lshl_add_u64 v[2:3], s[36:37], 0, v[178:179]
	v_lshl_add_u64 v[2:3], v[2:3], 0, s[14:15]
	s_addc_u32 s3, s11, 0
	s_add_i32 s62, s50, 0x8000
	global_load_lds_dwordx4 v[2:3], off
	s_mov_b32 m0, s62
	s_add_i32 s63, s50, 0xa000
	s_mov_b64 s[16:17], 0x36000080
	global_load_lds_dwordx4 v180, s[2:3]
	s_mov_b32 m0, s63
	s_mov_b32 s61, 0x8000
	global_load_lds_dwordx4 v182, s[2:3]
	s_add_u32 s2, s36, 0x4080
	s_addc_u32 s3, s37, 0
	s_add_i32 m0, s50, 0x1c000
	s_movk_i32 s64, 0x100
	global_load_lds_dwordx4 v176, s[2:3]
	s_add_i32 m0, s50, 0x1e000
	v_mov_b32_e32 v184, v176
	global_load_lds_dwordx4 v178, s[2:3]
	s_waitcnt vmcnt(6)
	v_readlane_b32 s2, v254, 15
	s_cmpk_lt_u32 s2, 0x100
	s_cselect_b64 s[18:19], -1, 0
	s_add_i32 s65, s45, -1
	v_mov_b32_e32 v231, 0x24854
	v_mov_b32_e32 v252, 0x24858
	v_mov_b32_e32 v253, 0x2485c
	v_mov_b32_e32 v220, 0x24864
	v_mov_b32_e32 v221, 0x24868
	v_mov_b32_e32 v222, 0x2486c
	v_mov_b32_e32 v223, 0x24870
	v_mov_b32_e32 v224, 0x24874
	v_mov_b32_e32 v225, 0x24878
	v_mov_b32_e32 v226, 0x2487c
	s_mov_b32 s66, 0x25800
	s_add_i32 s67, 0, 0x10000
	s_add_i32 s68, 0, 0x14000
	v_add_u32_e32 v227, 0, v6
	v_add_u32_e32 v228, 0, v5
	v_mov_b32_e32 v229, 0x7f7f7f7f
	v_add_u32_e32 v220, 0x10000, v194
	v_add_u32_e32 v221, 0x10000, v195
	v_add_u32_e32 v222, 0x14000, v194
	v_add_u32_e32 v223, 0x14000, v195
	v_add_u32_e32 v224, 0x18000, v194
	v_add_u32_e32 v225, 0x18000, v195
	v_add_u32_e32 v226, 0x1c000, v194
	v_add_u32_e32 v229, 0x1c000, v195
	s_mov_b64 s[20:21], 0x5e000000
	s_mov_b32 s69, 0xc0c00000
	s_mov_b64 s[22:23], 0x22000000
	s_mov_b32 s70, 0x22001000
	v_mov_b32_e32 v230, 0x41000000
	v_mov_b32_e32 v176, v0
	s_mov_b32 s74, 0
	v_mov_b32_e32 v0, v177
	v_mov_b32_e32 v1, v177
	v_mov_b32_e32 v2, v177
	v_mov_b32_e32 v3, v177
	v_mov_b32_e32 v4, v177
	v_mov_b32_e32 v5, v177
	v_mov_b32_e32 v6, v177
	v_mov_b32_e32 v7, v177
	v_mov_b32_e32 v8, v177
	v_mov_b32_e32 v9, v177
	v_mov_b32_e32 v10, v177
	v_mov_b32_e32 v11, v177
	v_mov_b32_e32 v12, v177
	v_mov_b32_e32 v13, v177
	v_mov_b32_e32 v14, v177
	v_mov_b32_e32 v15, v177
	v_mov_b32_e32 v16, v177
	v_mov_b32_e32 v17, v177
	v_mov_b32_e32 v18, v177
	v_mov_b32_e32 v19, v177
	v_mov_b32_e32 v20, v177
	v_mov_b32_e32 v21, v177
	v_mov_b32_e32 v22, v177
	v_mov_b32_e32 v23, v177
	v_mov_b32_e32 v24, v177
	v_mov_b32_e32 v25, v177
	v_mov_b32_e32 v26, v177
	v_mov_b32_e32 v27, v177
	v_mov_b32_e32 v28, v177
	v_mov_b32_e32 v29, v177
	v_mov_b32_e32 v30, v177
	v_mov_b32_e32 v31, v177
	v_mov_b32_e32 v36, v177
	v_mov_b32_e32 v37, v177
	v_mov_b32_e32 v38, v177
	v_mov_b32_e32 v39, v177
	v_mov_b32_e32 v44, v177
	v_mov_b32_e32 v45, v177
	v_mov_b32_e32 v46, v177
	v_mov_b32_e32 v47, v177
	v_mov_b32_e32 v32, v177
	v_mov_b32_e32 v33, v177
	v_mov_b32_e32 v34, v177
	v_mov_b32_e32 v35, v177
	v_mov_b32_e32 v40, v177
	v_mov_b32_e32 v41, v177
	v_mov_b32_e32 v42, v177
	v_mov_b32_e32 v43, v177
	v_mov_b32_e32 v48, v177
	v_mov_b32_e32 v49, v177
	v_mov_b32_e32 v50, v177
	v_mov_b32_e32 v51, v177
	v_mov_b32_e32 v52, v177
	v_mov_b32_e32 v53, v177
	v_mov_b32_e32 v54, v177
	v_mov_b32_e32 v55, v177
	v_mov_b32_e32 v56, v177
	v_mov_b32_e32 v57, v177
	v_mov_b32_e32 v58, v177
	v_mov_b32_e32 v59, v177
	v_mov_b32_e32 v60, v177
	v_mov_b32_e32 v61, v177
	v_mov_b32_e32 v62, v177
	v_mov_b32_e32 v63, v177
	v_mov_b32_e32 v64, v177
	v_mov_b32_e32 v65, v177
	v_mov_b32_e32 v66, v177
	v_mov_b32_e32 v67, v177
	v_mov_b32_e32 v68, v177
	v_mov_b32_e32 v69, v177
	v_mov_b32_e32 v70, v177
	v_mov_b32_e32 v71, v177
	v_mov_b32_e32 v72, v177
	v_mov_b32_e32 v73, v177
	v_mov_b32_e32 v74, v177
	v_mov_b32_e32 v75, v177
	v_mov_b32_e32 v76, v177
	v_mov_b32_e32 v77, v177
	v_mov_b32_e32 v78, v177
	v_mov_b32_e32 v79, v177
	v_mov_b32_e32 v80, v177
	v_mov_b32_e32 v81, v177
	v_mov_b32_e32 v82, v177
	v_mov_b32_e32 v83, v177
	v_mov_b32_e32 v84, v177
	v_mov_b32_e32 v85, v177
	v_mov_b32_e32 v86, v177
	v_mov_b32_e32 v87, v177
	v_mov_b32_e32 v88, v177
	v_mov_b32_e32 v89, v177
	v_mov_b32_e32 v90, v177
	v_mov_b32_e32 v91, v177
	v_mov_b32_e32 v92, v177
	v_mov_b32_e32 v93, v177
	v_mov_b32_e32 v94, v177
	v_mov_b32_e32 v95, v177
	v_mov_b32_e32 v96, v177
	v_mov_b32_e32 v97, v177
	v_mov_b32_e32 v98, v177
	v_mov_b32_e32 v99, v177
	v_mov_b32_e32 v100, v177
	v_mov_b32_e32 v101, v177
	v_mov_b32_e32 v102, v177
	v_mov_b32_e32 v103, v177
	v_mov_b32_e32 v104, v177
	v_mov_b32_e32 v105, v177
	v_mov_b32_e32 v106, v177
	v_mov_b32_e32 v107, v177
	v_mov_b32_e32 v108, v177
	v_mov_b32_e32 v109, v177
	v_mov_b32_e32 v110, v177
	v_mov_b32_e32 v111, v177
	v_mov_b32_e32 v112, v177
	v_mov_b32_e32 v113, v177
	v_mov_b32_e32 v114, v177
	v_mov_b32_e32 v115, v177
	v_mov_b32_e32 v116, v177
	v_mov_b32_e32 v117, v177
	v_mov_b32_e32 v118, v177
	v_mov_b32_e32 v119, v177
	v_mov_b32_e32 v120, v177
	v_mov_b32_e32 v121, v177
	v_mov_b32_e32 v122, v177
	v_mov_b32_e32 v123, v177
	v_mov_b32_e32 v124, v177
	v_mov_b32_e32 v125, v177
	v_mov_b32_e32 v126, v177
	v_mov_b32_e32 v127, v177
	s_barrier

.LBB0_910:
	s_add_u32 s25, s36, 0x100
	s_addc_u32 s27, s37, 0
	s_lshl_b32 s7, s55, 10
	s_add_i32 s7, s7, 0x24000
	s_mov_b32 s42, -2
	s_mov_b64 s[36:37], 0
	s_cmp_eq_u32 s42, 12
	s_cselect_b64 s[40:41], -1, 0
	s_and_b64 s[38:39], s[34:35], s[40:41]
	s_andn2_b64 vcc, exec, s[38:39]
	v_mov_b32_e32 v128, v186
	v_mov_b32_e32 v129, v176
	s_add_u32 s76, s10, s36
	s_addc_u32 s77, s11, s37
	ds_read_b128 v[130:133], v220
	ds_read_b128 v[138:141], v220 offset:2048
	ds_read_b128 v[134:137], v221
	ds_read_b128 v[142:145], v221 offset:2048
	ds_read_b128 v[146:149], v222
	ds_read_b128 v[154:157], v222 offset:2048
	ds_read_b128 v[150:153], v223
	ds_read_b128 v[158:161], v223 offset:2048
	s_add_u32 s43, s76, 0x36000100
	s_addc_u32 s75, s77, 0
	s_and_b64 s[38:39], s[40:41], exec
	s_cselect_b32 s39, s13, s75
	s_cselect_b32 s38, s12, s43
	s_add_u32 s43, s25, s36
	s_addc_u32 s75, s27, s37
	s_and_b64 s[40:41], s[40:41], exec
	s_cselect_b32 s41, s31, s75
	s_cselect_b32 s40, s30, s43
	ds_read_b128 v[162:165], v227
	ds_read_b128 v[232:235], v227 offset:2048
	ds_read_b128 v[166:169], v228
	ds_read_b128 v[236:239], v228 offset:2048
	ds_read_b128 v[240:243], v227 offset:4096
	ds_read_b128 v[196:199], v227 offset:6144
	ds_read_b128 v[244:247], v228 offset:4096
	ds_read_b128 v[200:203], v228 offset:6144
	s_add_i32 m0, s50, 0xc000
	s_add_u32 vcc_lo, s76, s16
	s_addc_u32 vcc_hi, s77, s17
	global_load_lds_dwordx4 v176, vcc
	s_add_i32 m0, s50, 0xe000
	s_nop 0
	global_load_lds_dwordx4 v186, vcc
	s_waitcnt vmcnt(8)
	s_waitcnt lgkmcnt(0)
	s_barrier
	s_setprio 1
	s_waitcnt lgkmcnt(0)
	v_mfma_f32_16x16x128_f8f6f4 v[100:103], v[130:137], v[162:169], 0
	v_mfma_f32_16x16x128_f8f6f4 v[96:99], v[138:145], v[162:169], 0
	v_mfma_f32_16x16x128_f8f6f4 v[92:95], v[130:137], v[232:239], 0
	v_mfma_f32_16x16x128_f8f6f4 v[88:91], v[138:145], v[232:239], 0
	v_mfma_f32_16x16x128_f8f6f4 v[84:87], v[130:137], v[240:247], 0
	v_mfma_f32_16x16x128_f8f6f4 v[80:83], v[138:145], v[240:247], 0
	v_mfma_f32_16x16x128_f8f6f4 v[170:173], v[130:137], v[196:203], 0
	v_mfma_f32_16x16x128_f8f6f4 v[188:191], v[138:145], v[196:203], 0
	s_setprio 0
	s_setprio 1
	v_mfma_f32_16x16x128_f8f6f4 v[40:43], v[146:153], v[196:203], 0
	v_mfma_f32_16x16x128_f8f6f4 v[32:35], v[154:161], v[196:203], 0
	v_mfma_f32_16x16x128_f8f6f4 v[248:251], v[146:153], v[162:169], 0
	v_mfma_f32_16x16x128_f8f6f4 v[204:207], v[154:161], v[162:169], 0
	v_mfma_f32_16x16x128_f8f6f4 v[208:211], v[146:153], v[232:239], 0
	v_mfma_f32_16x16x128_f8f6f4 v[212:215], v[154:161], v[232:239], 0
	v_mfma_f32_16x16x128_f8f6f4 v[216:219], v[146:153], v[240:247], 0
	v_mfma_f32_16x16x128_f8f6f4 v[240:243], v[154:161], v[240:247], 0
	s_setprio 0
	s_barrier
	s_add_i32 s43, s67, s5
	s_mov_b32 m0, s43
	s_nop 2
	ds_read_b128 v[48:51], v227 offset:16384
	ds_read_b128 v[56:59], v227 offset:18432
	ds_read_b128 v[52:55], v228 offset:16384
	ds_read_b128 v[60:63], v228 offset:18432
	ds_read_b128 v[64:67], v227 offset:20480
	ds_read_b128 v[72:75], v227 offset:22528
	ds_read_b128 v[68:71], v228 offset:20480
	ds_read_b128 v[76:79], v228 offset:22528
	s_nop 0
	global_load_lds_dwordx4 v184, s[40:41]
	s_add_i32 m0, s43, 0x2000
	s_add_u32 s76, s40, 0x4000
	s_addc_u32 s77, s41, 0
	s_add_i32 s43, s68, s5
	s_nop 0
	global_load_lds_dwordx4 v178, s[40:41]
	s_mov_b32 m0, s43
	s_nop 0
	global_load_lds_dwordx4 v184, s[76:77]
	s_add_i32 m0, s43, 0x2000
	s_nop 0
	global_load_lds_dwordx4 v178, s[76:77]
	s_waitcnt vmcnt(6)
	s_waitcnt lgkmcnt(0)
	s_barrier
	s_setprio 1
	s_waitcnt lgkmcnt(0)
	v_mfma_f32_16x16x128_f8f6f4 v[44:47], v[130:137], v[48:55], 0
	v_mfma_f32_16x16x128_f8f6f4 v[36:39], v[138:145], v[48:55], 0
	v_mfma_f32_16x16x128_f8f6f4 v[28:31], v[130:137], v[56:63], 0
	v_mfma_f32_16x16x128_f8f6f4 v[24:27], v[138:145], v[56:63], 0
	v_mfma_f32_16x16x128_f8f6f4 v[20:23], v[130:137], v[64:71], 0
	v_mfma_f32_16x16x128_f8f6f4 v[16:19], v[138:145], v[64:71], 0
	v_mfma_f32_16x16x128_f8f6f4 v[12:15], v[130:137], v[72:79], 0
	v_mfma_f32_16x16x128_f8f6f4 v[8:11], v[138:145], v[72:79], 0
	s_setprio 0
	s_setprio 1
	v_mfma_f32_16x16x128_f8f6f4 v[4:7], v[146:153], v[48:55], 0
	v_mfma_f32_16x16x128_f8f6f4 v[0:3], v[154:161], v[48:55], 0
	v_mfma_f32_16x16x128_f8f6f4 v[104:107], v[146:153], v[56:63], 0
	v_mfma_f32_16x16x128_f8f6f4 v[108:111], v[154:161], v[56:63], 0
	v_mfma_f32_16x16x128_f8f6f4 v[112:115], v[146:153], v[64:71], 0
	v_mfma_f32_16x16x128_f8f6f4 v[116:119], v[154:161], v[64:71], 0
	v_mfma_f32_16x16x128_f8f6f4 v[120:123], v[146:153], v[72:79], 0
	v_mfma_f32_16x16x128_f8f6f4 v[124:127], v[154:161], v[72:79], 0
	s_setprio 0
	s_barrier
	s_add_i32 s43, 0, 0x18000
	s_add_i32 s75, 0, 0x1c000
	ds_read_b128 v[130:133], v224
	ds_read_b128 v[138:141], v224 offset:2048
	ds_read_b128 v[134:137], v225
	ds_read_b128 v[142:145], v225 offset:2048
	ds_read_b128 v[146:149], v226
	ds_read_b128 v[154:157], v226 offset:2048
	ds_read_b128 v[150:153], v229
	ds_read_b128 v[158:161], v229 offset:2048
	s_mov_b32 m0, s52
	v_mov_b32_e32 v176, v129
	ds_read_b128 v[48:51], v227 offset:32768
	ds_read_b128 v[162:165], v227 offset:34816
	ds_read_b128 v[52:55], v228 offset:32768
	ds_read_b128 v[166:169], v228 offset:34816
	ds_read_b128 v[196:199], v227 offset:36864
	ds_read_b128 v[232:235], v227 offset:38912
	ds_read_b128 v[200:203], v228 offset:36864
	ds_read_b128 v[236:239], v228 offset:38912
	s_mov_b32 m0, s50
	s_nop 0
	global_load_lds_dwordx4 v180, s[38:39]
	s_mov_b32 m0, s51
	s_nop 0
	global_load_lds_dwordx4 v182, s[38:39]
	s_mov_b32 m0, s52
	v_mov_b32_e32 v186, v128
	global_load_lds_dwordx4 v176, s[38:39]
	s_mov_b32 m0, s53
	s_nop 0
	global_load_lds_dwordx4 v186, s[38:39]
	s_waitcnt vmcnt(8)
	s_waitcnt lgkmcnt(0)
	s_barrier
	s_setprio 1
	s_waitcnt lgkmcnt(0)
	v_mfma_f32_16x16x128_f8f6f4 v[100:103], v[130:137], v[48:55], v[100:103]
	v_mfma_f32_16x16x128_f8f6f4 v[96:99], v[138:145], v[48:55], v[96:99]
	v_mfma_f32_16x16x128_f8f6f4 v[92:95], v[130:137], v[162:169], v[92:95]
	v_mfma_f32_16x16x128_f8f6f4 v[88:91], v[138:145], v[162:169], v[88:91]
	v_mfma_f32_16x16x128_f8f6f4 v[84:87], v[130:137], v[196:203], v[84:87]
	v_mfma_f32_16x16x128_f8f6f4 v[80:83], v[138:145], v[196:203], v[80:83]
	v_mfma_f32_16x16x128_f8f6f4 v[76:79], v[130:137], v[232:239], v[170:173]
	v_mfma_f32_16x16x128_f8f6f4 v[72:75], v[138:145], v[232:239], v[188:191]
	s_setprio 0
	s_setprio 1
	v_mfma_f32_16x16x128_f8f6f4 v[68:71], v[146:153], v[48:55], v[248:251]
	v_mfma_f32_16x16x128_f8f6f4 v[64:67], v[154:161], v[48:55], v[204:207]
	v_mfma_f32_16x16x128_f8f6f4 v[60:63], v[146:153], v[162:169], v[208:211]
	v_mfma_f32_16x16x128_f8f6f4 v[56:59], v[154:161], v[162:169], v[212:215]
	v_mfma_f32_16x16x128_f8f6f4 v[52:55], v[146:153], v[196:203], v[216:219]
	v_mfma_f32_16x16x128_f8f6f4 v[48:51], v[154:161], v[196:203], v[240:243]
	v_mfma_f32_16x16x128_f8f6f4 v[40:43], v[146:153], v[232:239], v[40:43]
	v_mfma_f32_16x16x128_f8f6f4 v[32:35], v[154:161], v[232:239], v[32:35]
	s_setprio 0
	s_barrier
	ds_read_b128 v[162:165], v227 offset:49152
	ds_read_b128 v[196:199], v227 offset:51200
	ds_read_b128 v[166:169], v228 offset:49152
	ds_read_b128 v[200:203], v228 offset:51200
	ds_read_b128 v[232:235], v227 offset:53248
	ds_read_b128 v[240:243], v227 offset:55296
	ds_read_b128 v[236:239], v228 offset:53248
	ds_read_b128 v[244:247], v228 offset:55296
	s_add_i32 s43, s43, s5
	s_add_u32 vcc_lo, s40, s14
	s_addc_u32 vcc_hi, s41, s15
	s_mov_b32 m0, s43
	global_load_lds_dwordx4 v184, vcc
	s_add_i32 m0, s43, 0x2000
	s_add_u32 s40, s40, 0x4080
	s_addc_u32 s41, s41, 0
	s_add_i32 s43, s75, s5
	global_load_lds_dwordx4 v178, vcc
	s_mov_b32 m0, s43
	global_load_lds_dwordx4 v184, s[40:41]
	s_add_i32 m0, s43, 0x2000
	s_nop 0
	global_load_lds_dwordx4 v178, s[40:41]
	s_mov_b32 m0, s62
	s_add_u32 vcc_lo, s38, s14
	s_addc_u32 vcc_hi, s39, s15
	global_load_lds_dwordx4 v180, vcc
	s_mov_b32 m0, s63
	s_nop 0
	global_load_lds_dwordx4 v182, vcc
	s_waitcnt vmcnt(8)
	s_waitcnt lgkmcnt(0)
	s_barrier
	s_setprio 1
	s_waitcnt lgkmcnt(0)
	v_mfma_f32_16x16x128_f8f6f4 v[44:47], v[130:137], v[162:169], v[44:47]
	v_mfma_f32_16x16x128_f8f6f4 v[36:39], v[138:145], v[162:169], v[36:39]
	v_mfma_f32_16x16x128_f8f6f4 v[28:31], v[130:137], v[196:203], v[28:31]
	v_mfma_f32_16x16x128_f8f6f4 v[24:27], v[138:145], v[196:203], v[24:27]
	v_mfma_f32_16x16x128_f8f6f4 v[20:23], v[130:137], v[232:239], v[20:23]
	v_mfma_f32_16x16x128_f8f6f4 v[16:19], v[138:145], v[232:239], v[16:19]
	v_mfma_f32_16x16x128_f8f6f4 v[12:15], v[130:137], v[240:247], v[12:15]
	v_mfma_f32_16x16x128_f8f6f4 v[8:11], v[138:145], v[240:247], v[8:11]
	s_setprio 0
	s_setprio 1
	v_mfma_f32_16x16x128_f8f6f4 v[4:7], v[146:153], v[162:169], v[4:7]
	v_mfma_f32_16x16x128_f8f6f4 v[0:3], v[154:161], v[162:169], v[0:3]
	v_mfma_f32_16x16x128_f8f6f4 v[104:107], v[146:153], v[196:203], v[104:107]
	v_mfma_f32_16x16x128_f8f6f4 v[108:111], v[154:161], v[196:203], v[108:111]
	v_mfma_f32_16x16x128_f8f6f4 v[112:115], v[146:153], v[232:239], v[112:115]
	v_mfma_f32_16x16x128_f8f6f4 v[116:119], v[154:161], v[232:239], v[116:119]
	v_mfma_f32_16x16x128_f8f6f4 v[120:123], v[146:153], v[240:247], v[120:123]
	v_mfma_f32_16x16x128_f8f6f4 v[124:127], v[154:161], v[240:247], v[124:127]
	s_setprio 0
	s_barrier
	s_add_i32 s42, s42, 2
	s_add_u32 s36, s36, 0x100
	s_addc_u32 s37, s37, 0
	s_branch .LBB0_912
.LBB0_911:
	s_add_u32 s76, s10, s36
	s_addc_u32 s77, s11, s37
	ds_read_b128 v[130:133], v220
	ds_read_b128 v[138:141], v220 offset:2048
	ds_read_b128 v[134:137], v221
	ds_read_b128 v[142:145], v221 offset:2048
	ds_read_b128 v[146:149], v222
	ds_read_b128 v[154:157], v222 offset:2048
	ds_read_b128 v[150:153], v223
	ds_read_b128 v[158:161], v223 offset:2048
	s_add_u32 s43, s76, 0x36000100
	s_addc_u32 s75, s77, 0
	s_and_b64 s[38:39], s[40:41], exec
	s_cselect_b32 s39, s13, s75
	s_cselect_b32 s38, s12, s43
	s_add_u32 s43, s25, s36
	s_addc_u32 s75, s27, s37
	s_and_b64 s[40:41], s[40:41], exec
	s_cselect_b32 s41, s31, s75
	s_cselect_b32 s40, s30, s43
	ds_read_b128 v[162:165], v227
	ds_read_b128 v[232:235], v227 offset:2048
	ds_read_b128 v[166:169], v228
	ds_read_b128 v[236:239], v228 offset:2048
	ds_read_b128 v[240:243], v227 offset:4096
	ds_read_b128 v[196:199], v227 offset:6144
	ds_read_b128 v[244:247], v228 offset:4096
	ds_read_b128 v[200:203], v228 offset:6144
	s_add_i32 m0, s50, 0xc000
	s_add_u32 vcc_lo, s76, s16
	s_addc_u32 vcc_hi, s77, s17
	global_load_lds_dwordx4 v176, vcc
	s_add_i32 m0, s50, 0xe000
	s_nop 0
	global_load_lds_dwordx4 v186, vcc
	s_waitcnt vmcnt(8)
	s_waitcnt lgkmcnt(0)
	s_barrier
	s_setprio 1
	s_waitcnt lgkmcnt(0)
	v_mfma_f32_16x16x128_f8f6f4 v[100:103], v[130:137], v[162:169], v[100:103]
	v_mfma_f32_16x16x128_f8f6f4 v[96:99], v[138:145], v[162:169], v[96:99]
	v_mfma_f32_16x16x128_f8f6f4 v[92:95], v[130:137], v[232:239], v[92:95]
	v_mfma_f32_16x16x128_f8f6f4 v[88:91], v[138:145], v[232:239], v[88:91]
	v_mfma_f32_16x16x128_f8f6f4 v[84:87], v[130:137], v[240:247], v[84:87]
	v_mfma_f32_16x16x128_f8f6f4 v[80:83], v[138:145], v[240:247], v[80:83]
	v_mfma_f32_16x16x128_f8f6f4 v[170:173], v[130:137], v[196:203], v[76:79]
	v_mfma_f32_16x16x128_f8f6f4 v[188:191], v[138:145], v[196:203], v[72:75]
	s_setprio 0
	s_setprio 1
	v_mfma_f32_16x16x128_f8f6f4 v[40:43], v[146:153], v[196:203], v[40:43]
	v_mfma_f32_16x16x128_f8f6f4 v[32:35], v[154:161], v[196:203], v[32:35]
	v_mfma_f32_16x16x128_f8f6f4 v[248:251], v[146:153], v[162:169], v[68:71]
	v_mfma_f32_16x16x128_f8f6f4 v[204:207], v[154:161], v[162:169], v[64:67]
	v_mfma_f32_16x16x128_f8f6f4 v[208:211], v[146:153], v[232:239], v[60:63]
	v_mfma_f32_16x16x128_f8f6f4 v[212:215], v[154:161], v[232:239], v[56:59]
	v_mfma_f32_16x16x128_f8f6f4 v[216:219], v[146:153], v[240:247], v[52:55]
	v_mfma_f32_16x16x128_f8f6f4 v[240:243], v[154:161], v[240:247], v[48:51]
	s_setprio 0
	s_barrier
	s_add_i32 s43, s67, s5
	s_mov_b32 m0, s43
	s_nop 2
	ds_read_b128 v[48:51], v227 offset:16384
	ds_read_b128 v[56:59], v227 offset:18432
	ds_read_b128 v[52:55], v228 offset:16384
	ds_read_b128 v[60:63], v228 offset:18432
	ds_read_b128 v[64:67], v227 offset:20480
	ds_read_b128 v[72:75], v227 offset:22528
	ds_read_b128 v[68:71], v228 offset:20480
	ds_read_b128 v[76:79], v228 offset:22528
	s_nop 0
	global_load_lds_dwordx4 v184, s[40:41]
	s_add_i32 m0, s43, 0x2000
	s_add_u32 s76, s40, 0x4000
	s_addc_u32 s77, s41, 0
	s_add_i32 s43, s68, s5
	s_nop 0
	global_load_lds_dwordx4 v178, s[40:41]
	s_mov_b32 m0, s43
	s_nop 0
	global_load_lds_dwordx4 v184, s[76:77]
	s_add_i32 m0, s43, 0x2000
	s_nop 0
	global_load_lds_dwordx4 v178, s[76:77]
	s_waitcnt vmcnt(6)
	s_waitcnt lgkmcnt(0)
	s_barrier
	s_setprio 1
	s_waitcnt lgkmcnt(0)
	v_mfma_f32_16x16x128_f8f6f4 v[44:47], v[130:137], v[48:55], v[44:47]
	v_mfma_f32_16x16x128_f8f6f4 v[36:39], v[138:145], v[48:55], v[36:39]
	v_mfma_f32_16x16x128_f8f6f4 v[28:31], v[130:137], v[56:63], v[28:31]
	v_mfma_f32_16x16x128_f8f6f4 v[24:27], v[138:145], v[56:63], v[24:27]
	v_mfma_f32_16x16x128_f8f6f4 v[20:23], v[130:137], v[64:71], v[20:23]
	v_mfma_f32_16x16x128_f8f6f4 v[16:19], v[138:145], v[64:71], v[16:19]
	v_mfma_f32_16x16x128_f8f6f4 v[12:15], v[130:137], v[72:79], v[12:15]
	v_mfma_f32_16x16x128_f8f6f4 v[8:11], v[138:145], v[72:79], v[8:11]
	s_setprio 0
	s_setprio 1
	v_mfma_f32_16x16x128_f8f6f4 v[4:7], v[146:153], v[48:55], v[4:7]
	v_mfma_f32_16x16x128_f8f6f4 v[0:3], v[154:161], v[48:55], v[0:3]
	v_mfma_f32_16x16x128_f8f6f4 v[104:107], v[146:153], v[56:63], v[104:107]
	v_mfma_f32_16x16x128_f8f6f4 v[108:111], v[154:161], v[56:63], v[108:111]
	v_mfma_f32_16x16x128_f8f6f4 v[112:115], v[146:153], v[64:71], v[112:115]
	v_mfma_f32_16x16x128_f8f6f4 v[116:119], v[154:161], v[64:71], v[116:119]
	v_mfma_f32_16x16x128_f8f6f4 v[120:123], v[146:153], v[72:79], v[120:123]
	v_mfma_f32_16x16x128_f8f6f4 v[124:127], v[154:161], v[72:79], v[124:127]
	s_setprio 0
	s_barrier
	s_add_i32 s43, 0, 0x18000
	s_add_i32 s75, 0, 0x1c000
	ds_read_b128 v[130:133], v224
	ds_read_b128 v[138:141], v224 offset:2048
	ds_read_b128 v[134:137], v225
	ds_read_b128 v[142:145], v225 offset:2048
	ds_read_b128 v[146:149], v226
	ds_read_b128 v[154:157], v226 offset:2048
	ds_read_b128 v[150:153], v229
	ds_read_b128 v[158:161], v229 offset:2048
	s_mov_b32 m0, s52
	v_mov_b32_e32 v176, v129
	ds_read_b128 v[48:51], v227 offset:32768
	ds_read_b128 v[162:165], v227 offset:34816
	ds_read_b128 v[52:55], v228 offset:32768
	ds_read_b128 v[166:169], v228 offset:34816
	ds_read_b128 v[196:199], v227 offset:36864
	ds_read_b128 v[232:235], v227 offset:38912
	ds_read_b128 v[200:203], v228 offset:36864
	ds_read_b128 v[236:239], v228 offset:38912
	s_mov_b32 m0, s50
	s_nop 0
	global_load_lds_dwordx4 v180, s[38:39]
	s_mov_b32 m0, s51
	s_nop 0
	global_load_lds_dwordx4 v182, s[38:39]
	s_mov_b32 m0, s52
	v_mov_b32_e32 v186, v128
	global_load_lds_dwordx4 v176, s[38:39]
	s_mov_b32 m0, s53
	s_nop 0
	global_load_lds_dwordx4 v186, s[38:39]
	s_waitcnt vmcnt(8)
	s_waitcnt lgkmcnt(0)
	s_barrier
	s_setprio 1
	s_waitcnt lgkmcnt(0)
	v_mfma_f32_16x16x128_f8f6f4 v[100:103], v[130:137], v[48:55], v[100:103]
	v_mfma_f32_16x16x128_f8f6f4 v[96:99], v[138:145], v[48:55], v[96:99]
	v_mfma_f32_16x16x128_f8f6f4 v[92:95], v[130:137], v[162:169], v[92:95]
	v_mfma_f32_16x16x128_f8f6f4 v[88:91], v[138:145], v[162:169], v[88:91]
	v_mfma_f32_16x16x128_f8f6f4 v[84:87], v[130:137], v[196:203], v[84:87]
	v_mfma_f32_16x16x128_f8f6f4 v[80:83], v[138:145], v[196:203], v[80:83]
	v_mfma_f32_16x16x128_f8f6f4 v[76:79], v[130:137], v[232:239], v[170:173]
	v_mfma_f32_16x16x128_f8f6f4 v[72:75], v[138:145], v[232:239], v[188:191]
	s_setprio 0
	s_setprio 1
	v_mfma_f32_16x16x128_f8f6f4 v[68:71], v[146:153], v[48:55], v[248:251]
	v_mfma_f32_16x16x128_f8f6f4 v[64:67], v[154:161], v[48:55], v[204:207]
	v_mfma_f32_16x16x128_f8f6f4 v[60:63], v[146:153], v[162:169], v[208:211]
	v_mfma_f32_16x16x128_f8f6f4 v[56:59], v[154:161], v[162:169], v[212:215]
	v_mfma_f32_16x16x128_f8f6f4 v[52:55], v[146:153], v[196:203], v[216:219]
	v_mfma_f32_16x16x128_f8f6f4 v[48:51], v[154:161], v[196:203], v[240:243]
	v_mfma_f32_16x16x128_f8f6f4 v[40:43], v[146:153], v[232:239], v[40:43]
	v_mfma_f32_16x16x128_f8f6f4 v[32:35], v[154:161], v[232:239], v[32:35]
	s_setprio 0
	s_barrier
	ds_read_b128 v[162:165], v227 offset:49152
	ds_read_b128 v[196:199], v227 offset:51200
	ds_read_b128 v[166:169], v228 offset:49152
	ds_read_b128 v[200:203], v228 offset:51200
	ds_read_b128 v[232:235], v227 offset:53248
	ds_read_b128 v[240:243], v227 offset:55296
	ds_read_b128 v[236:239], v228 offset:53248
	ds_read_b128 v[244:247], v228 offset:55296
	s_add_i32 s43, s43, s5
	s_add_u32 vcc_lo, s40, s14
	s_addc_u32 vcc_hi, s41, s15
	s_mov_b32 m0, s43
	global_load_lds_dwordx4 v184, vcc
	s_add_i32 m0, s43, 0x2000
	s_add_u32 s40, s40, 0x4080
	s_addc_u32 s41, s41, 0
	s_add_i32 s43, s75, s5
	global_load_lds_dwordx4 v178, vcc
	s_mov_b32 m0, s43
	global_load_lds_dwordx4 v184, s[40:41]
	s_add_i32 m0, s43, 0x2000
	s_nop 0
	global_load_lds_dwordx4 v178, s[40:41]
	s_mov_b32 m0, s62
	s_add_u32 vcc_lo, s38, s14
	s_addc_u32 vcc_hi, s39, s15
	global_load_lds_dwordx4 v180, vcc
	s_mov_b32 m0, s63
	s_nop 0
	global_load_lds_dwordx4 v182, vcc
	s_waitcnt vmcnt(8)
	s_waitcnt lgkmcnt(0)
	s_barrier
	s_setprio 1
	s_waitcnt lgkmcnt(0)
	v_mfma_f32_16x16x128_f8f6f4 v[44:47], v[130:137], v[162:169], v[44:47]
	v_mfma_f32_16x16x128_f8f6f4 v[36:39], v[138:145], v[162:169], v[36:39]
	v_mfma_f32_16x16x128_f8f6f4 v[28:31], v[130:137], v[196:203], v[28:31]
	v_mfma_f32_16x16x128_f8f6f4 v[24:27], v[138:145], v[196:203], v[24:27]
	v_mfma_f32_16x16x128_f8f6f4 v[20:23], v[130:137], v[232:239], v[20:23]
	v_mfma_f32_16x16x128_f8f6f4 v[16:19], v[138:145], v[232:239], v[16:19]
	v_mfma_f32_16x16x128_f8f6f4 v[12:15], v[130:137], v[240:247], v[12:15]
	v_mfma_f32_16x16x128_f8f6f4 v[8:11], v[138:145], v[240:247], v[8:11]
	s_setprio 0
	s_setprio 1
	v_mfma_f32_16x16x128_f8f6f4 v[4:7], v[146:153], v[162:169], v[4:7]
	v_mfma_f32_16x16x128_f8f6f4 v[0:3], v[154:161], v[162:169], v[0:3]
	v_mfma_f32_16x16x128_f8f6f4 v[104:107], v[146:153], v[196:203], v[104:107]
	v_mfma_f32_16x16x128_f8f6f4 v[108:111], v[154:161], v[196:203], v[108:111]
	v_mfma_f32_16x16x128_f8f6f4 v[112:115], v[146:153], v[232:239], v[112:115]
	v_mfma_f32_16x16x128_f8f6f4 v[116:119], v[154:161], v[232:239], v[116:119]
	v_mfma_f32_16x16x128_f8f6f4 v[120:123], v[146:153], v[240:247], v[120:123]
	v_mfma_f32_16x16x128_f8f6f4 v[124:127], v[154:161], v[240:247], v[124:127]
	s_setprio 0
	s_barrier
	s_add_i32 s42, s42, 2
	s_add_u32 s36, s36, 0x100
	s_addc_u32 s37, s37, 0
	s_cmp_gt_u32 s42, 13
	s_cbranch_scc1 .LBB0_914
